# attention: PV split into two key-half passes; the second half's exp/rowsum/bf16 packing is interleaved between the first pass's MFMAs; V fragments streamed in 16 units with 3-unit lookahead
# speedup vs baseline: 1.1751x; 1.0047x over previous
.Lfa_nodma:
	s_waitcnt lgkmcnt(2)
	v_mfma_f32_32x32x16_bf16 v[130:145], v[228:231], v[162:165], 0
	v_mfma_f32_32x32x16_bf16 v[146:161], v[232:235], v[162:165], 0
	ds_read_b128 v[228:231], v246 offset:0
	ds_read_b128 v[232:235], v246 offset:8192
	s_waitcnt lgkmcnt(2)
	v_mfma_f32_32x32x16_bf16 v[130:145], v[236:239], v[166:169], v[130:145]
	v_mfma_f32_32x32x16_bf16 v[146:161], v[240:243], v[166:169], v[146:161]
	ds_read_b128 v[236:239], v247 offset:0
	ds_read_b128 v[240:243], v247 offset:8192
	s_waitcnt lgkmcnt(2)
	v_mfma_f32_32x32x16_bf16 v[130:145], v[228:231], v[170:173], v[130:145]
	v_mfma_f32_32x32x16_bf16 v[146:161], v[232:235], v[170:173], v[146:161]
	ds_read_b128 v[228:231], v244 offset:128
	ds_read_b128 v[232:235], v244 offset:8320
	s_waitcnt lgkmcnt(2)
	v_mfma_f32_32x32x16_bf16 v[130:145], v[236:239], v[174:177], v[130:145]
	v_mfma_f32_32x32x16_bf16 v[146:161], v[240:243], v[174:177], v[146:161]
	ds_read_b128 v[236:239], v245 offset:128
	ds_read_b128 v[240:243], v245 offset:8320
	s_waitcnt lgkmcnt(2)
	v_mfma_f32_32x32x16_bf16 v[130:145], v[228:231], v[178:181], v[130:145]
	v_mfma_f32_32x32x16_bf16 v[146:161], v[232:235], v[178:181], v[146:161]
	ds_read_b128 v[228:231], v246 offset:128
	ds_read_b128 v[232:235], v246 offset:8320
	s_waitcnt lgkmcnt(2)
	v_mfma_f32_32x32x16_bf16 v[130:145], v[236:239], v[182:185], v[130:145]
	v_mfma_f32_32x32x16_bf16 v[146:161], v[240:243], v[182:185], v[146:161]
	ds_read_b128 v[236:239], v247 offset:128
	ds_read_b128 v[240:243], v247 offset:8320
	s_waitcnt lgkmcnt(2)
	v_mfma_f32_32x32x16_bf16 v[130:145], v[228:231], v[186:189], v[130:145]
	v_mfma_f32_32x32x16_bf16 v[146:161], v[232:235], v[186:189], v[146:161]
	s_waitcnt lgkmcnt(0)
	v_mfma_f32_32x32x16_bf16 v[130:145], v[236:239], v[190:193], v[130:145]
	v_mfma_f32_32x32x16_bf16 v[146:161], v[240:243], v[190:193], v[146:161]
	v_add_u32_e32 v253, s84, v210
	ds_read_b64_tr_b16 v[228:229], v253 offset:0
	ds_read_b64_tr_b16 v[230:231], v253 offset:2048
	ds_read_b64_tr_b16 v[232:233], v253 offset:4096
	ds_read_b64_tr_b16 v[234:235], v253 offset:6144
	ds_read_b64_tr_b16 v[236:237], v253 offset:512
	ds_read_b64_tr_b16 v[238:239], v253 offset:2560
	ds_read_b64_tr_b16 v[240:241], v253 offset:4608
	ds_read_b64_tr_b16 v[242:243], v253 offset:6656
	ds_read_b64_tr_b16 v[244:245], v253 offset:1024
	ds_read_b64_tr_b16 v[246:247], v253 offset:3072
	ds_read_b64_tr_b16 v[248:249], v253 offset:5120
	ds_read_b64_tr_b16 v[250:251], v253 offset:7168
	s_cmp_ge_u32 s4, s14
	s_cbranch_scc0 .Lfa_nomask
	v_mbcnt_lo_u32_b32 v206, -1, 0
	v_mbcnt_hi_u32_b32 v206, -1, v206
	v_and_b32_e32 v203, 31, v206
	v_lshrrev_b32_e32 v206, 5, v206
	v_lshlrev_b32_e32 v206, 2, v206
	v_sub_u32_e32 v203, v203, v206
	s_lshl_b32 s21, s4, 6
	s_sub_i32 s21, s24, s21
	v_add_u32_e32 v203, s21, v203
	v_mov_b32_e32 v204, 0xff800000
	v_cmp_gt_i32_e64 vcc, 0, v203
	v_cmp_gt_i32_e64 s[48:49], 32, v203
	v_cmp_gt_i32_e64 s[50:51], 1, v203
	v_cmp_gt_i32_e64 s[52:53], 33, v203
	v_cndmask_b32_e64 v130, v130, v204, vcc
	v_cndmask_b32_e64 v146, v146, v204, s[48:49]
	v_cndmask_b32_e64 v131, v131, v204, s[50:51]
	v_cndmask_b32_e64 v147, v147, v204, s[52:53]
	v_cmp_gt_i32_e64 vcc, 2, v203
	v_cmp_gt_i32_e64 s[48:49], 34, v203
	v_cmp_gt_i32_e64 s[50:51], 3, v203
	v_cmp_gt_i32_e64 s[52:53], 35, v203
	v_cndmask_b32_e64 v132, v132, v204, vcc
	v_cndmask_b32_e64 v148, v148, v204, s[48:49]
	v_cndmask_b32_e64 v133, v133, v204, s[50:51]
	v_cndmask_b32_e64 v149, v149, v204, s[52:53]
	v_cmp_gt_i32_e64 vcc, 8, v203
	v_cmp_gt_i32_e64 s[48:49], 40, v203
	v_cmp_gt_i32_e64 s[50:51], 9, v203
	v_cmp_gt_i32_e64 s[52:53], 41, v203
	v_cndmask_b32_e64 v134, v134, v204, vcc
	v_cndmask_b32_e64 v150, v150, v204, s[48:49]
	v_cndmask_b32_e64 v135, v135, v204, s[50:51]
	v_cndmask_b32_e64 v151, v151, v204, s[52:53]
	v_cmp_gt_i32_e64 vcc, 10, v203
	v_cmp_gt_i32_e64 s[48:49], 42, v203
	v_cmp_gt_i32_e64 s[50:51], 11, v203
	v_cmp_gt_i32_e64 s[52:53], 43, v203
	v_cndmask_b32_e64 v136, v136, v204, vcc
	v_cndmask_b32_e64 v152, v152, v204, s[48:49]
	v_cndmask_b32_e64 v137, v137, v204, s[50:51]
	v_cndmask_b32_e64 v153, v153, v204, s[52:53]
	v_cmp_gt_i32_e64 vcc, 16, v203
	v_cmp_gt_i32_e64 s[48:49], 48, v203
	v_cmp_gt_i32_e64 s[50:51], 17, v203
	v_cmp_gt_i32_e64 s[52:53], 49, v203
	v_cndmask_b32_e64 v138, v138, v204, vcc
	v_cndmask_b32_e64 v154, v154, v204, s[48:49]
	v_cndmask_b32_e64 v139, v139, v204, s[50:51]
	v_cndmask_b32_e64 v155, v155, v204, s[52:53]
	v_cmp_gt_i32_e64 vcc, 18, v203
	v_cmp_gt_i32_e64 s[48:49], 50, v203
	v_cmp_gt_i32_e64 s[50:51], 19, v203
	v_cmp_gt_i32_e64 s[52:53], 51, v203
	v_cndmask_b32_e64 v140, v140, v204, vcc
	v_cndmask_b32_e64 v156, v156, v204, s[48:49]
	v_cndmask_b32_e64 v141, v141, v204, s[50:51]
	v_cndmask_b32_e64 v157, v157, v204, s[52:53]
	v_cmp_gt_i32_e64 vcc, 24, v203
	v_cmp_gt_i32_e64 s[48:49], 56, v203
	v_cmp_gt_i32_e64 s[50:51], 25, v203
	v_cmp_gt_i32_e64 s[52:53], 57, v203
	v_cndmask_b32_e64 v142, v142, v204, vcc
	v_cndmask_b32_e64 v158, v158, v204, s[48:49]
	v_cndmask_b32_e64 v143, v143, v204, s[50:51]
	v_cndmask_b32_e64 v159, v159, v204, s[52:53]
	v_cmp_gt_i32_e64 vcc, 26, v203
	v_cmp_gt_i32_e64 s[48:49], 58, v203
	v_cmp_gt_i32_e64 s[50:51], 27, v203
	v_cmp_gt_i32_e64 s[52:53], 59, v203
	v_cndmask_b32_e64 v144, v144, v204, vcc
	v_cndmask_b32_e64 v160, v160, v204, s[48:49]
	v_cndmask_b32_e64 v145, v145, v204, s[50:51]
	v_cndmask_b32_e64 v161, v161, v204, s[52:53]
.Lfa_nomask:
	v_max3_f32 v203, v130, v131, v132
	v_max3_f32 v203, v203, v133, v134
	v_max3_f32 v203, v203, v135, v136
	v_max3_f32 v203, v203, v137, v138
	v_max3_f32 v203, v203, v139, v140
	v_max3_f32 v203, v203, v141, v142
	v_max3_f32 v203, v203, v143, v144
	v_max3_f32 v203, v203, v145, v146
	v_max3_f32 v203, v203, v147, v148
	v_max3_f32 v203, v203, v149, v150
	v_max3_f32 v203, v203, v151, v152
	v_max3_f32 v203, v203, v153, v154
	v_max3_f32 v203, v203, v155, v156
	v_max3_f32 v203, v203, v157, v158
	v_max3_f32 v203, v203, v159, v160
	v_max_f32_e32 v203, v203, v161
	v_mov_b32_e32 v204, v203
	s_nop 1
	v_permlane32_swap_b32_e32 v203, v204
	v_max_f32_e32 v203, v203, v204
	v_sub_f32_e32 v204, v203, v96
	v_mov_b32_e32 v207, 0x42b504f3
	v_cmp_gt_f32_e32 vcc, v204, v207
	s_cmp_lg_u64 vcc, 0
	s_cselect_b64 s[92:93], -1, 0
	v_max_f32_e32 v204, v96, v203
	s_nop 0
	v_cndmask_b32_e64 v207, v96, v204, s[92:93]
	v_sub_f32_e32 v206, v96, v207
	v_mul_f32_e32 v206, 0x3e0293ee, v206
	v_exp_f32_e32 v206, v206
	v_mov_b32_e32 v96, v207
	v_mul_f32_e32 v207, 0xbe0293ee, v207
	v_mov_b32_e32 v204, 0x3e0293ee
	v_mul_f32_e32 v202, v202, v206
	v_fma_f32 v130, v130, v204, v207
	v_fma_f32 v131, v131, v204, v207
	v_fma_f32 v132, v132, v204, v207
	v_fma_f32 v133, v133, v204, v207
	v_fma_f32 v134, v134, v204, v207
	v_fma_f32 v135, v135, v204, v207
	v_fma_f32 v136, v136, v204, v207
	v_fma_f32 v137, v137, v204, v207
	v_fma_f32 v138, v138, v204, v207
	v_fma_f32 v139, v139, v204, v207
	v_fma_f32 v140, v140, v204, v207
	v_fma_f32 v141, v141, v204, v207
	v_fma_f32 v142, v142, v204, v207
	v_fma_f32 v143, v143, v204, v207
	v_fma_f32 v144, v144, v204, v207
	v_fma_f32 v145, v145, v204, v207
	v_fma_f32 v146, v146, v204, v207
	v_fma_f32 v147, v147, v204, v207
	v_fma_f32 v148, v148, v204, v207
	v_fma_f32 v149, v149, v204, v207
	v_fma_f32 v150, v150, v204, v207
	v_fma_f32 v151, v151, v204, v207
	v_fma_f32 v152, v152, v204, v207
	v_fma_f32 v153, v153, v204, v207
	v_fma_f32 v154, v154, v204, v207
	v_fma_f32 v155, v155, v204, v207
	v_fma_f32 v156, v156, v204, v207
	v_fma_f32 v157, v157, v204, v207
	v_fma_f32 v158, v158, v204, v207
	v_fma_f32 v159, v159, v204, v207
	v_fma_f32 v160, v160, v204, v207
	v_fma_f32 v161, v161, v204, v207
	v_exp_f32_e32 v130, v130
	v_exp_f32_e32 v131, v131
	v_exp_f32_e32 v132, v132
	v_exp_f32_e32 v133, v133
	v_exp_f32_e32 v134, v134
	v_exp_f32_e32 v135, v135
	v_exp_f32_e32 v136, v136
	v_exp_f32_e32 v137, v137
	v_exp_f32_e32 v138, v138
	v_exp_f32_e32 v139, v139
	v_exp_f32_e32 v140, v140
	v_exp_f32_e32 v141, v141
	v_exp_f32_e32 v142, v142
	v_exp_f32_e32 v143, v143
	v_exp_f32_e32 v144, v144
	v_exp_f32_e32 v145, v145
	s_nop 0
	v_add_f32_e32 v252, v130, v131
	v_add_f32_e32 v252, v252, v132
	v_add_f32_e32 v252, v252, v133
	v_add_f32_e32 v252, v252, v134
	v_add_f32_e32 v252, v252, v135
	v_add_f32_e32 v252, v252, v136
	v_add_f32_e32 v252, v252, v137
	v_add_f32_e32 v252, v252, v138
	v_add_f32_e32 v252, v252, v139
	v_add_f32_e32 v252, v252, v140
	v_add_f32_e32 v252, v252, v141
	v_add_f32_e32 v252, v252, v142
	v_add_f32_e32 v252, v252, v143
	v_add_f32_e32 v252, v252, v144
	v_add_f32_e32 v252, v252, v145
	v_cvt_pk_bf16_f32 v212, v130, v131
	v_cvt_pk_bf16_f32 v213, v132, v133
	v_cvt_pk_bf16_f32 v214, v134, v135
	v_cvt_pk_bf16_f32 v215, v136, v137
	v_cvt_pk_bf16_f32 v216, v138, v139
	v_cvt_pk_bf16_f32 v217, v140, v141
	v_cvt_pk_bf16_f32 v218, v142, v143
	v_cvt_pk_bf16_f32 v219, v144, v145
	s_nop 1
	v_permlane32_swap_b32_e32 v212, v214
	v_permlane32_swap_b32_e32 v213, v215
	v_permlane32_swap_b32_e32 v216, v218
	v_permlane32_swap_b32_e32 v217, v219
	s_and_b64 vcc, exec, s[92:93]
	s_cbranch_vccz .Lfa_noresc_t
	v_mbcnt_lo_u32_b32 v204, -1, 0
	v_mbcnt_hi_u32_b32 v204, -1, v204
	s_lshl_b32 s21, s15, 8
	s_add_i32 s21, s21, 0x18000
	v_and_b32_e32 v207, 31, v204
	v_lshl_add_u32 v207, v207, 2, s21
	v_lshrrev_b32_e32 v204, 5, v204
	v_lshl_add_u32 v204, v204, 4, s21
	ds_write_b32 v207, v206
	s_waitcnt lgkmcnt(0)
	ds_read_b128 v[236:239], v204 offset:0
	ds_read_b128 v[240:243], v204 offset:32
	ds_read_b128 v[244:247], v204 offset:64
	ds_read_b128 v[248:251], v204 offset:96
	s_waitcnt lgkmcnt(0)
	v_pk_mul_f32 v[0:1], v[0:1], v[236:237]
	v_pk_mul_f32 v[2:3], v[2:3], v[238:239]
	v_pk_mul_f32 v[4:5], v[4:5], v[240:241]
	v_pk_mul_f32 v[6:7], v[6:7], v[242:243]
	v_pk_mul_f32 v[8:9], v[8:9], v[244:245]
	v_pk_mul_f32 v[10:11], v[10:11], v[246:247]
	v_pk_mul_f32 v[12:13], v[12:13], v[248:249]
	v_pk_mul_f32 v[14:15], v[14:15], v[250:251]
	v_pk_mul_f32 v[16:17], v[16:17], v[236:237]
	v_pk_mul_f32 v[18:19], v[18:19], v[238:239]
	v_pk_mul_f32 v[20:21], v[20:21], v[240:241]
	v_pk_mul_f32 v[22:23], v[22:23], v[242:243]
	v_pk_mul_f32 v[24:25], v[24:25], v[244:245]
	v_pk_mul_f32 v[26:27], v[26:27], v[246:247]
	v_pk_mul_f32 v[28:29], v[28:29], v[248:249]
	v_pk_mul_f32 v[30:31], v[30:31], v[250:251]
	v_pk_mul_f32 v[32:33], v[32:33], v[236:237]
	v_pk_mul_f32 v[34:35], v[34:35], v[238:239]
	v_pk_mul_f32 v[36:37], v[36:37], v[240:241]
	v_pk_mul_f32 v[38:39], v[38:39], v[242:243]
	v_pk_mul_f32 v[40:41], v[40:41], v[244:245]
	v_pk_mul_f32 v[42:43], v[42:43], v[246:247]
	v_pk_mul_f32 v[44:45], v[44:45], v[248:249]
	v_pk_mul_f32 v[46:47], v[46:47], v[250:251]
	v_pk_mul_f32 v[48:49], v[48:49], v[236:237]
	v_pk_mul_f32 v[50:51], v[50:51], v[238:239]
	v_pk_mul_f32 v[52:53], v[52:53], v[240:241]
	v_pk_mul_f32 v[54:55], v[54:55], v[242:243]
	v_pk_mul_f32 v[56:57], v[56:57], v[244:245]
	v_pk_mul_f32 v[58:59], v[58:59], v[246:247]
	v_pk_mul_f32 v[60:61], v[60:61], v[248:249]
	v_pk_mul_f32 v[62:63], v[62:63], v[250:251]
	v_pk_mul_f32 v[64:65], v[64:65], v[236:237]
	v_pk_mul_f32 v[66:67], v[66:67], v[238:239]
	v_pk_mul_f32 v[68:69], v[68:69], v[240:241]
	v_pk_mul_f32 v[70:71], v[70:71], v[242:243]
	v_pk_mul_f32 v[72:73], v[72:73], v[244:245]
	v_pk_mul_f32 v[74:75], v[74:75], v[246:247]
	v_pk_mul_f32 v[76:77], v[76:77], v[248:249]
	v_pk_mul_f32 v[78:79], v[78:79], v[250:251]
	v_pk_mul_f32 v[80:81], v[80:81], v[236:237]
	v_pk_mul_f32 v[82:83], v[82:83], v[238:239]
	v_pk_mul_f32 v[84:85], v[84:85], v[240:241]
	v_pk_mul_f32 v[86:87], v[86:87], v[242:243]
	v_pk_mul_f32 v[88:89], v[88:89], v[244:245]
	v_pk_mul_f32 v[90:91], v[90:91], v[246:247]
	v_pk_mul_f32 v[92:93], v[92:93], v[248:249]
	v_pk_mul_f32 v[94:95], v[94:95], v[250:251]
	v_pk_mul_f32 v[98:99], v[98:99], v[236:237]
	v_pk_mul_f32 v[100:101], v[100:101], v[238:239]
	v_pk_mul_f32 v[102:103], v[102:103], v[240:241]
	v_pk_mul_f32 v[104:105], v[104:105], v[242:243]
	v_pk_mul_f32 v[106:107], v[106:107], v[244:245]
	v_pk_mul_f32 v[108:109], v[108:109], v[246:247]
	v_pk_mul_f32 v[110:111], v[110:111], v[248:249]
	v_pk_mul_f32 v[112:113], v[112:113], v[250:251]
	v_pk_mul_f32 v[114:115], v[114:115], v[236:237]
	v_pk_mul_f32 v[116:117], v[116:117], v[238:239]
	v_pk_mul_f32 v[118:119], v[118:119], v[240:241]
	v_pk_mul_f32 v[120:121], v[120:121], v[242:243]
	v_pk_mul_f32 v[122:123], v[122:123], v[244:245]
	v_pk_mul_f32 v[124:125], v[124:125], v[246:247]
	v_pk_mul_f32 v[126:127], v[126:127], v[248:249]
	v_pk_mul_f32 v[128:129], v[128:129], v[250:251]
	ds_read_b64_tr_b16 v[228:229], v253 offset:0
	ds_read_b64_tr_b16 v[230:231], v253 offset:2048
	ds_read_b64_tr_b16 v[232:233], v253 offset:4096
	ds_read_b64_tr_b16 v[234:235], v253 offset:6144
	ds_read_b64_tr_b16 v[236:237], v253 offset:512
	ds_read_b64_tr_b16 v[238:239], v253 offset:2560
	ds_read_b64_tr_b16 v[240:241], v253 offset:4608
	ds_read_b64_tr_b16 v[242:243], v253 offset:6656
	ds_read_b64_tr_b16 v[244:245], v253 offset:1024
	ds_read_b64_tr_b16 v[246:247], v253 offset:3072
	ds_read_b64_tr_b16 v[248:249], v253 offset:5120
	ds_read_b64_tr_b16 v[250:251], v253 offset:7168
.Lfa_noresc_t:
	s_waitcnt lgkmcnt(8)
	v_mfma_f32_32x32x16_bf16 v[0:15], v[212:215], v[228:231], v[0:15]
	v_exp_f32_e32 v146, v146
	v_exp_f32_e32 v147, v147
	v_mfma_f32_32x32x16_bf16 v[0:15], v[216:219], v[232:235], v[0:15]
	v_exp_f32_e32 v148, v148
	v_exp_f32_e32 v149, v149
	ds_read_b64_tr_b16 v[194:195], v253 offset:1536
	ds_read_b64_tr_b16 v[196:197], v253 offset:3584
	ds_read_b64_tr_b16 v[198:199], v253 offset:5632
	ds_read_b64_tr_b16 v[200:201], v253 offset:7680
	s_waitcnt lgkmcnt(8)
	v_mfma_f32_32x32x16_bf16 v[16:31], v[212:215], v[236:239], v[16:31]
	v_exp_f32_e32 v150, v150
	v_add_f32_e32 v252, v252, v146
	v_exp_f32_e32 v151, v151
	v_mfma_f32_32x32x16_bf16 v[16:31], v[216:219], v[240:243], v[16:31]
	v_add_f32_e32 v252, v252, v147
	v_exp_f32_e32 v152, v152
	v_add_f32_e32 v252, v252, v148
	ds_read_b64_tr_b16 v[228:229], v253 offset:16384
	ds_read_b64_tr_b16 v[230:231], v253 offset:18432
	ds_read_b64_tr_b16 v[232:233], v253 offset:20480
	ds_read_b64_tr_b16 v[234:235], v253 offset:22528
	s_waitcnt lgkmcnt(8)
	v_mfma_f32_32x32x16_bf16 v[32:47], v[212:215], v[244:247], v[32:47]
	v_exp_f32_e32 v153, v153
	v_add_f32_e32 v252, v252, v149
	v_exp_f32_e32 v154, v154
	v_mfma_f32_32x32x16_bf16 v[32:47], v[216:219], v[248:251], v[32:47]
	v_add_f32_e32 v252, v252, v150
	v_exp_f32_e32 v155, v155
	v_add_f32_e32 v252, v252, v151
	ds_read_b64_tr_b16 v[236:237], v253 offset:16896
	ds_read_b64_tr_b16 v[238:239], v253 offset:18944
	ds_read_b64_tr_b16 v[240:241], v253 offset:20992
	ds_read_b64_tr_b16 v[242:243], v253 offset:23040
	s_waitcnt lgkmcnt(8)
	v_mfma_f32_32x32x16_bf16 v[48:63], v[212:215], v[194:197], v[48:63]
	v_exp_f32_e32 v156, v156
	v_add_f32_e32 v252, v252, v152
	v_exp_f32_e32 v157, v157
	v_mfma_f32_32x32x16_bf16 v[48:63], v[216:219], v[198:201], v[48:63]
	v_add_f32_e32 v252, v252, v153
	v_exp_f32_e32 v158, v158
	v_add_f32_e32 v252, v252, v154
	ds_read_b64_tr_b16 v[244:245], v253 offset:17408
	ds_read_b64_tr_b16 v[246:247], v253 offset:19456
	ds_read_b64_tr_b16 v[248:249], v253 offset:21504
	ds_read_b64_tr_b16 v[250:251], v253 offset:23552
	s_waitcnt lgkmcnt(8)
	v_mfma_f32_32x32x16_bf16 v[64:79], v[212:215], v[228:231], v[64:79]
	v_exp_f32_e32 v159, v159
	v_add_f32_e32 v252, v252, v155
	v_exp_f32_e32 v160, v160
	v_mfma_f32_32x32x16_bf16 v[64:79], v[216:219], v[232:235], v[64:79]
	v_add_f32_e32 v252, v252, v156
	v_exp_f32_e32 v161, v161
	v_add_f32_e32 v252, v252, v157
	v_add_f32_e32 v252, v252, v158
	v_add_f32_e32 v252, v252, v159
	v_add_f32_e32 v252, v252, v160
	ds_read_b64_tr_b16 v[194:195], v253 offset:17920
	ds_read_b64_tr_b16 v[196:197], v253 offset:19968
	ds_read_b64_tr_b16 v[198:199], v253 offset:22016
	ds_read_b64_tr_b16 v[200:201], v253 offset:24064
	s_waitcnt lgkmcnt(8)
	v_mfma_f32_32x32x16_bf16 v[80:95], v[212:215], v[236:239], v[80:95]
	v_add_f32_e32 v252, v252, v161
	v_mov_b32_e32 v204, v252
	s_nop 1
	v_permlane32_swap_b32_e32 v252, v204
	v_add_f32_e32 v252, v252, v204
	v_add_f32_e32 v202, v202, v252
	v_cvt_pk_bf16_f32 v220, v146, v147
	v_cvt_pk_bf16_f32 v221, v148, v149
	v_cvt_pk_bf16_f32 v222, v150, v151
	v_mfma_f32_32x32x16_bf16 v[80:95], v[216:219], v[240:243], v[80:95]
	v_cvt_pk_bf16_f32 v223, v152, v153
	v_cvt_pk_bf16_f32 v224, v154, v155
	v_cvt_pk_bf16_f32 v225, v156, v157
	v_cvt_pk_bf16_f32 v226, v158, v159
	v_cvt_pk_bf16_f32 v227, v160, v161
	s_nop 1
	v_permlane32_swap_b32_e32 v220, v222
	v_permlane32_swap_b32_e32 v221, v223
	v_permlane32_swap_b32_e32 v224, v226
	ds_read_b64_tr_b16 v[228:229], v253 offset:8192
	ds_read_b64_tr_b16 v[230:231], v253 offset:10240
	ds_read_b64_tr_b16 v[232:233], v253 offset:12288
	ds_read_b64_tr_b16 v[234:235], v253 offset:14336
	s_waitcnt lgkmcnt(8)
	v_mfma_f32_32x32x16_bf16 v[98:113], v[212:215], v[244:247], v[98:113]
	v_permlane32_swap_b32_e32 v225, v227
	v_mfma_f32_32x32x16_bf16 v[98:113], v[216:219], v[248:251], v[98:113]
	ds_read_b64_tr_b16 v[236:237], v253 offset:8704
	ds_read_b64_tr_b16 v[238:239], v253 offset:10752
	ds_read_b64_tr_b16 v[240:241], v253 offset:12800
	ds_read_b64_tr_b16 v[242:243], v253 offset:14848
	s_waitcnt lgkmcnt(8)
	v_mfma_f32_32x32x16_bf16 v[114:129], v[212:215], v[194:197], v[114:129]
	v_mfma_f32_32x32x16_bf16 v[114:129], v[216:219], v[198:201], v[114:129]
	ds_read_b64_tr_b16 v[244:245], v253 offset:9216
	ds_read_b64_tr_b16 v[246:247], v253 offset:11264
	ds_read_b64_tr_b16 v[248:249], v253 offset:13312
	ds_read_b64_tr_b16 v[250:251], v253 offset:15360
	s_nop 1
	s_waitcnt lgkmcnt(8)
	v_mfma_f32_32x32x16_bf16 v[0:15], v[220:223], v[228:231], v[0:15]
	v_mfma_f32_32x32x16_bf16 v[0:15], v[224:227], v[232:235], v[0:15]
	ds_read_b64_tr_b16 v[194:195], v253 offset:9728
	ds_read_b64_tr_b16 v[196:197], v253 offset:11776
	ds_read_b64_tr_b16 v[198:199], v253 offset:13824
	ds_read_b64_tr_b16 v[200:201], v253 offset:15872
	s_waitcnt lgkmcnt(8)
	v_mfma_f32_32x32x16_bf16 v[16:31], v[220:223], v[236:239], v[16:31]
	v_mfma_f32_32x32x16_bf16 v[16:31], v[224:227], v[240:243], v[16:31]
	ds_read_b64_tr_b16 v[228:229], v253 offset:24576
	ds_read_b64_tr_b16 v[230:231], v253 offset:26624
	ds_read_b64_tr_b16 v[232:233], v253 offset:28672
	ds_read_b64_tr_b16 v[234:235], v253 offset:30720
	s_waitcnt lgkmcnt(8)
	v_mfma_f32_32x32x16_bf16 v[32:47], v[220:223], v[244:247], v[32:47]
	v_mfma_f32_32x32x16_bf16 v[32:47], v[224:227], v[248:251], v[32:47]
	ds_read_b64_tr_b16 v[236:237], v253 offset:25088
	ds_read_b64_tr_b16 v[238:239], v253 offset:27136
	ds_read_b64_tr_b16 v[240:241], v253 offset:29184
	ds_read_b64_tr_b16 v[242:243], v253 offset:31232
	s_waitcnt lgkmcnt(8)
	v_mfma_f32_32x32x16_bf16 v[48:63], v[220:223], v[194:197], v[48:63]
	v_mfma_f32_32x32x16_bf16 v[48:63], v[224:227], v[198:201], v[48:63]
	ds_read_b64_tr_b16 v[244:245], v253 offset:25600
	ds_read_b64_tr_b16 v[246:247], v253 offset:27648
	ds_read_b64_tr_b16 v[248:249], v253 offset:29696
	ds_read_b64_tr_b16 v[250:251], v253 offset:31744
	s_waitcnt lgkmcnt(8)
	v_mfma_f32_32x32x16_bf16 v[64:79], v[220:223], v[228:231], v[64:79]
	v_mfma_f32_32x32x16_bf16 v[64:79], v[224:227], v[232:235], v[64:79]
	ds_read_b64_tr_b16 v[194:195], v253 offset:26112
	ds_read_b64_tr_b16 v[196:197], v253 offset:28160
	ds_read_b64_tr_b16 v[198:199], v253 offset:30208
	ds_read_b64_tr_b16 v[200:201], v253 offset:32256
	s_waitcnt lgkmcnt(8)
	v_mfma_f32_32x32x16_bf16 v[80:95], v[220:223], v[236:239], v[80:95]
	v_mfma_f32_32x32x16_bf16 v[80:95], v[224:227], v[240:243], v[80:95]
	s_waitcnt lgkmcnt(4)
	v_mfma_f32_32x32x16_bf16 v[98:113], v[220:223], v[244:247], v[98:113]
	v_mfma_f32_32x32x16_bf16 v[98:113], v[224:227], v[248:251], v[98:113]
	s_waitcnt lgkmcnt(0)
	v_mfma_f32_32x32x16_bf16 v[114:129], v[220:223], v[194:197], v[114:129]
	v_mfma_f32_32x32x16_bf16 v[114:129], v[224:227], v[198:201], v[114:129]
	s_add_i32 s4, s4, 1
	s_cmp_lt_u32 s4, s5
	s_cbranch_scc1 .Lfa_tile
	s_bitcmp1_b32 s9, 0
	s_cbranch_scc1 .Lfa_epi_c1
	s_nop 7
	s_nop 7
	v_mbcnt_lo_u32_b32 v229, -1, 0
	v_mbcnt_hi_u32_b32 v229, -1, v229
	s_lshl_b32 s21, s15, 8
	s_add_i32 s21, s21, 0x18000
	v_and_b32_e32 v231, 31, v229
	v_lshl_add_u32 v230, v231, 2, s21
	v_lshrrev_b32_e32 v229, 5, v229
	v_lshl_add_u32 v232, v229, 4, s21
	ds_write_b32 v230, v202 offset:128
	s_waitcnt lgkmcnt(0)
	ds_read_b128 v[236:239], v232 offset:128
	ds_read_b128 v[240:243], v232 offset:160
	ds_read_b128 v[244:247], v232 offset:192
	ds_read_b128 v[248:251], v232 offset:224
	s_waitcnt lgkmcnt(0)
	v_rcp_f32_e32 v236, v236
	v_rcp_f32_e32 v237, v237
	v_rcp_f32_e32 v238, v238
	v_rcp_f32_e32 v239, v239
	v_rcp_f32_e32 v240, v240
	v_rcp_f32_e32 v241, v241
	v_rcp_f32_e32 v242, v242
	v_rcp_f32_e32 v243, v243
	v_rcp_f32_e32 v244, v244
	v_rcp_f32_e32 v245, v245
	v_rcp_f32_e32 v246, v246
	v_rcp_f32_e32 v247, v247
	v_rcp_f32_e32 v248, v248
	v_rcp_f32_e32 v249, v249
	v_rcp_f32_e32 v250, v250
	v_rcp_f32_e32 v251, v251
	s_nop 0
	v_mul_f32_dpp v228, v0, v236 quad_perm:[1,0,3,2] row_mask:0xf bank_mask:0xf
	v_mul_f32_e32 v0, v0, v236
	v_cvt_pk_bf16_f32 v0, v0, v228
	v_mul_f32_dpp v228, v1, v237 quad_perm:[1,0,3,2] row_mask:0xf bank_mask:0xf
	v_mul_f32_e32 v1, v1, v237
	v_cvt_pk_bf16_f32 v1, v1, v228
	v_mul_f32_dpp v228, v2, v238 quad_perm:[1,0,3,2] row_mask:0xf bank_mask:0xf
	v_mul_f32_e32 v2, v2, v238
	v_cvt_pk_bf16_f32 v2, v2, v228
	v_mul_f32_dpp v228, v3, v239 quad_perm:[1,0,3,2] row_mask:0xf bank_mask:0xf
	v_mul_f32_e32 v3, v3, v239
	v_cvt_pk_bf16_f32 v3, v3, v228
	v_mul_f32_dpp v228, v4, v240 quad_perm:[1,0,3,2] row_mask:0xf bank_mask:0xf
	v_mul_f32_e32 v4, v4, v240
	v_cvt_pk_bf16_f32 v4, v4, v228
	v_mul_f32_dpp v228, v5, v241 quad_perm:[1,0,3,2] row_mask:0xf bank_mask:0xf
	v_mul_f32_e32 v5, v5, v241
	v_cvt_pk_bf16_f32 v5, v5, v228
	v_mul_f32_dpp v228, v6, v242 quad_perm:[1,0,3,2] row_mask:0xf bank_mask:0xf
	v_mul_f32_e32 v6, v6, v242
	v_cvt_pk_bf16_f32 v6, v6, v228
	v_mul_f32_dpp v228, v7, v243 quad_perm:[1,0,3,2] row_mask:0xf bank_mask:0xf
	v_mul_f32_e32 v7, v7, v243
	v_cvt_pk_bf16_f32 v7, v7, v228
	v_mul_f32_dpp v228, v8, v244 quad_perm:[1,0,3,2] row_mask:0xf bank_mask:0xf
	v_mul_f32_e32 v8, v8, v244
	v_cvt_pk_bf16_f32 v8, v8, v228
	v_mul_f32_dpp v228, v9, v245 quad_perm:[1,0,3,2] row_mask:0xf bank_mask:0xf
	v_mul_f32_e32 v9, v9, v245
	v_cvt_pk_bf16_f32 v9, v9, v228
	v_mul_f32_dpp v228, v10, v246 quad_perm:[1,0,3,2] row_mask:0xf bank_mask:0xf
	v_mul_f32_e32 v10, v10, v246
	v_cvt_pk_bf16_f32 v10, v10, v228
	v_mul_f32_dpp v228, v11, v247 quad_perm:[1,0,3,2] row_mask:0xf bank_mask:0xf
	v_mul_f32_e32 v11, v11, v247
	v_cvt_pk_bf16_f32 v11, v11, v228
	v_mul_f32_dpp v228, v12, v248 quad_perm:[1,0,3,2] row_mask:0xf bank_mask:0xf
	v_mul_f32_e32 v12, v12, v248
	v_cvt_pk_bf16_f32 v12, v12, v228
	v_mul_f32_dpp v228, v13, v249 quad_perm:[1,0,3,2] row_mask:0xf bank_mask:0xf
	v_mul_f32_e32 v13, v13, v249
	v_cvt_pk_bf16_f32 v13, v13, v228
	v_mul_f32_dpp v228, v14, v250 quad_perm:[1,0,3,2] row_mask:0xf bank_mask:0xf
	v_mul_f32_e32 v14, v14, v250
	v_cvt_pk_bf16_f32 v14, v14, v228
	v_mul_f32_dpp v228, v15, v251 quad_perm:[1,0,3,2] row_mask:0xf bank_mask:0xf
	v_mul_f32_e32 v15, v15, v251
	v_cvt_pk_bf16_f32 v15, v15, v228
	v_mul_f32_dpp v228, v16, v236 quad_perm:[1,0,3,2] row_mask:0xf bank_mask:0xf
	v_mul_f32_e32 v16, v16, v236
	v_cvt_pk_bf16_f32 v16, v16, v228
	v_mul_f32_dpp v228, v17, v237 quad_perm:[1,0,3,2] row_mask:0xf bank_mask:0xf
	v_mul_f32_e32 v17, v17, v237
	v_cvt_pk_bf16_f32 v17, v17, v228
	v_mul_f32_dpp v228, v18, v238 quad_perm:[1,0,3,2] row_mask:0xf bank_mask:0xf
	v_mul_f32_e32 v18, v18, v238
	v_cvt_pk_bf16_f32 v18, v18, v228
	v_mul_f32_dpp v228, v19, v239 quad_perm:[1,0,3,2] row_mask:0xf bank_mask:0xf
	v_mul_f32_e32 v19, v19, v239
	v_cvt_pk_bf16_f32 v19, v19, v228
	v_mul_f32_dpp v228, v20, v240 quad_perm:[1,0,3,2] row_mask:0xf bank_mask:0xf
	v_mul_f32_e32 v20, v20, v240
	v_cvt_pk_bf16_f32 v20, v20, v228
	v_mul_f32_dpp v228, v21, v241 quad_perm:[1,0,3,2] row_mask:0xf bank_mask:0xf
	v_mul_f32_e32 v21, v21, v241
	v_cvt_pk_bf16_f32 v21, v21, v228
	v_mul_f32_dpp v228, v22, v242 quad_perm:[1,0,3,2] row_mask:0xf bank_mask:0xf
	v_mul_f32_e32 v22, v22, v242
	v_cvt_pk_bf16_f32 v22, v22, v228
	v_mul_f32_dpp v228, v23, v243 quad_perm:[1,0,3,2] row_mask:0xf bank_mask:0xf
	v_mul_f32_e32 v23, v23, v243
	v_cvt_pk_bf16_f32 v23, v23, v228
	v_mul_f32_dpp v228, v24, v244 quad_perm:[1,0,3,2] row_mask:0xf bank_mask:0xf
	v_mul_f32_e32 v24, v24, v244
	v_cvt_pk_bf16_f32 v24, v24, v228
	v_mul_f32_dpp v228, v25, v245 quad_perm:[1,0,3,2] row_mask:0xf bank_mask:0xf
	v_mul_f32_e32 v25, v25, v245
	v_cvt_pk_bf16_f32 v25, v25, v228
	v_mul_f32_dpp v228, v26, v246 quad_perm:[1,0,3,2] row_mask:0xf bank_mask:0xf
	v_mul_f32_e32 v26, v26, v246
	v_cvt_pk_bf16_f32 v26, v26, v228
	v_mul_f32_dpp v228, v27, v247 quad_perm:[1,0,3,2] row_mask:0xf bank_mask:0xf
	v_mul_f32_e32 v27, v27, v247
	v_cvt_pk_bf16_f32 v27, v27, v228
	v_mul_f32_dpp v228, v28, v248 quad_perm:[1,0,3,2] row_mask:0xf bank_mask:0xf
	v_mul_f32_e32 v28, v28, v248
	v_cvt_pk_bf16_f32 v28, v28, v228
	v_mul_f32_dpp v228, v29, v249 quad_perm:[1,0,3,2] row_mask:0xf bank_mask:0xf
	v_mul_f32_e32 v29, v29, v249
	v_cvt_pk_bf16_f32 v29, v29, v228
	v_mul_f32_dpp v228, v30, v250 quad_perm:[1,0,3,2] row_mask:0xf bank_mask:0xf
	v_mul_f32_e32 v30, v30, v250
	v_cvt_pk_bf16_f32 v30, v30, v228
	v_mul_f32_dpp v228, v31, v251 quad_perm:[1,0,3,2] row_mask:0xf bank_mask:0xf
	v_mul_f32_e32 v31, v31, v251
	v_cvt_pk_bf16_f32 v31, v31, v228
	v_mul_f32_dpp v228, v32, v236 quad_perm:[1,0,3,2] row_mask:0xf bank_mask:0xf
	v_mul_f32_e32 v32, v32, v236
	v_cvt_pk_bf16_f32 v32, v32, v228
	v_mul_f32_dpp v228, v33, v237 quad_perm:[1,0,3,2] row_mask:0xf bank_mask:0xf
	v_mul_f32_e32 v33, v33, v237
	v_cvt_pk_bf16_f32 v33, v33, v228
	v_mul_f32_dpp v228, v34, v238 quad_perm:[1,0,3,2] row_mask:0xf bank_mask:0xf
	v_mul_f32_e32 v34, v34, v238
	v_cvt_pk_bf16_f32 v34, v34, v228
	v_mul_f32_dpp v228, v35, v239 quad_perm:[1,0,3,2] row_mask:0xf bank_mask:0xf
	v_mul_f32_e32 v35, v35, v239
	v_cvt_pk_bf16_f32 v35, v35, v228
	v_mul_f32_dpp v228, v36, v240 quad_perm:[1,0,3,2] row_mask:0xf bank_mask:0xf
	v_mul_f32_e32 v36, v36, v240
	v_cvt_pk_bf16_f32 v36, v36, v228
	v_mul_f32_dpp v228, v37, v241 quad_perm:[1,0,3,2] row_mask:0xf bank_mask:0xf
	v_mul_f32_e32 v37, v37, v241
	v_cvt_pk_bf16_f32 v37, v37, v228
	v_mul_f32_dpp v228, v38, v242 quad_perm:[1,0,3,2] row_mask:0xf bank_mask:0xf
	v_mul_f32_e32 v38, v38, v242
	v_cvt_pk_bf16_f32 v38, v38, v228
	v_mul_f32_dpp v228, v39, v243 quad_perm:[1,0,3,2] row_mask:0xf bank_mask:0xf
	v_mul_f32_e32 v39, v39, v243
	v_cvt_pk_bf16_f32 v39, v39, v228
	v_mul_f32_dpp v228, v40, v244 quad_perm:[1,0,3,2] row_mask:0xf bank_mask:0xf
	v_mul_f32_e32 v40, v40, v244
	v_cvt_pk_bf16_f32 v40, v40, v228
	v_mul_f32_dpp v228, v41, v245 quad_perm:[1,0,3,2] row_mask:0xf bank_mask:0xf
	v_mul_f32_e32 v41, v41, v245
	v_cvt_pk_bf16_f32 v41, v41, v228
	v_mul_f32_dpp v228, v42, v246 quad_perm:[1,0,3,2] row_mask:0xf bank_mask:0xf
	v_mul_f32_e32 v42, v42, v246
	v_cvt_pk_bf16_f32 v42, v42, v228
	v_mul_f32_dpp v228, v43, v247 quad_perm:[1,0,3,2] row_mask:0xf bank_mask:0xf
	v_mul_f32_e32 v43, v43, v247
	v_cvt_pk_bf16_f32 v43, v43, v228
	v_mul_f32_dpp v228, v44, v248 quad_perm:[1,0,3,2] row_mask:0xf bank_mask:0xf
	v_mul_f32_e32 v44, v44, v248
	v_cvt_pk_bf16_f32 v44, v44, v228
	v_mul_f32_dpp v228, v45, v249 quad_perm:[1,0,3,2] row_mask:0xf bank_mask:0xf
	v_mul_f32_e32 v45, v45, v249
	v_cvt_pk_bf16_f32 v45, v45, v228
	v_mul_f32_dpp v228, v46, v250 quad_perm:[1,0,3,2] row_mask:0xf bank_mask:0xf
	v_mul_f32_e32 v46, v46, v250
	v_cvt_pk_bf16_f32 v46, v46, v228
	v_mul_f32_dpp v228, v47, v251 quad_perm:[1,0,3,2] row_mask:0xf bank_mask:0xf
	v_mul_f32_e32 v47, v47, v251
	v_cvt_pk_bf16_f32 v47, v47, v228
	v_mul_f32_dpp v228, v48, v236 quad_perm:[1,0,3,2] row_mask:0xf bank_mask:0xf
	v_mul_f32_e32 v48, v48, v236
	v_cvt_pk_bf16_f32 v48, v48, v228
	v_mul_f32_dpp v228, v49, v237 quad_perm:[1,0,3,2] row_mask:0xf bank_mask:0xf
	v_mul_f32_e32 v49, v49, v237
	v_cvt_pk_bf16_f32 v49, v49, v228
	v_mul_f32_dpp v228, v50, v238 quad_perm:[1,0,3,2] row_mask:0xf bank_mask:0xf
	v_mul_f32_e32 v50, v50, v238
	v_cvt_pk_bf16_f32 v50, v50, v228
	v_mul_f32_dpp v228, v51, v239 quad_perm:[1,0,3,2] row_mask:0xf bank_mask:0xf
	v_mul_f32_e32 v51, v51, v239
	v_cvt_pk_bf16_f32 v51, v51, v228
	v_mul_f32_dpp v228, v52, v240 quad_perm:[1,0,3,2] row_mask:0xf bank_mask:0xf
	v_mul_f32_e32 v52, v52, v240
	v_cvt_pk_bf16_f32 v52, v52, v228
	v_mul_f32_dpp v228, v53, v241 quad_perm:[1,0,3,2] row_mask:0xf bank_mask:0xf
	v_mul_f32_e32 v53, v53, v241
	v_cvt_pk_bf16_f32 v53, v53, v228
	v_mul_f32_dpp v228, v54, v242 quad_perm:[1,0,3,2] row_mask:0xf bank_mask:0xf
	v_mul_f32_e32 v54, v54, v242
	v_cvt_pk_bf16_f32 v54, v54, v228
	v_mul_f32_dpp v228, v55, v243 quad_perm:[1,0,3,2] row_mask:0xf bank_mask:0xf
	v_mul_f32_e32 v55, v55, v243
	v_cvt_pk_bf16_f32 v55, v55, v228
	v_mul_f32_dpp v228, v56, v244 quad_perm:[1,0,3,2] row_mask:0xf bank_mask:0xf
	v_mul_f32_e32 v56, v56, v244
	v_cvt_pk_bf16_f32 v56, v56, v228
	v_mul_f32_dpp v228, v57, v245 quad_perm:[1,0,3,2] row_mask:0xf bank_mask:0xf
	v_mul_f32_e32 v57, v57, v245
	v_cvt_pk_bf16_f32 v57, v57, v228
	v_mul_f32_dpp v228, v58, v246 quad_perm:[1,0,3,2] row_mask:0xf bank_mask:0xf
	v_mul_f32_e32 v58, v58, v246
	v_cvt_pk_bf16_f32 v58, v58, v228
	v_mul_f32_dpp v228, v59, v247 quad_perm:[1,0,3,2] row_mask:0xf bank_mask:0xf
	v_mul_f32_e32 v59, v59, v247
	v_cvt_pk_bf16_f32 v59, v59, v228
	v_mul_f32_dpp v228, v60, v248 quad_perm:[1,0,3,2] row_mask:0xf bank_mask:0xf
	v_mul_f32_e32 v60, v60, v248
	v_cvt_pk_bf16_f32 v60, v60, v228
	v_mul_f32_dpp v228, v61, v249 quad_perm:[1,0,3,2] row_mask:0xf bank_mask:0xf
	v_mul_f32_e32 v61, v61, v249
	v_cvt_pk_bf16_f32 v61, v61, v228
	v_mul_f32_dpp v228, v62, v250 quad_perm:[1,0,3,2] row_mask:0xf bank_mask:0xf
	v_mul_f32_e32 v62, v62, v250
	v_cvt_pk_bf16_f32 v62, v62, v228
	v_mul_f32_dpp v228, v63, v251 quad_perm:[1,0,3,2] row_mask:0xf bank_mask:0xf
	v_mul_f32_e32 v63, v63, v251
	v_cvt_pk_bf16_f32 v63, v63, v228
	v_mul_f32_dpp v228, v64, v236 quad_perm:[1,0,3,2] row_mask:0xf bank_mask:0xf
	v_mul_f32_e32 v64, v64, v236
	v_cvt_pk_bf16_f32 v64, v64, v228
	v_mul_f32_dpp v228, v65, v237 quad_perm:[1,0,3,2] row_mask:0xf bank_mask:0xf
	v_mul_f32_e32 v65, v65, v237
	v_cvt_pk_bf16_f32 v65, v65, v228
	v_mul_f32_dpp v228, v66, v238 quad_perm:[1,0,3,2] row_mask:0xf bank_mask:0xf
	v_mul_f32_e32 v66, v66, v238
	v_cvt_pk_bf16_f32 v66, v66, v228
	v_mul_f32_dpp v228, v67, v239 quad_perm:[1,0,3,2] row_mask:0xf bank_mask:0xf
	v_mul_f32_e32 v67, v67, v239
	v_cvt_pk_bf16_f32 v67, v67, v228
	v_mul_f32_dpp v228, v68, v240 quad_perm:[1,0,3,2] row_mask:0xf bank_mask:0xf
	v_mul_f32_e32 v68, v68, v240
	v_cvt_pk_bf16_f32 v68, v68, v228
	v_mul_f32_dpp v228, v69, v241 quad_perm:[1,0,3,2] row_mask:0xf bank_mask:0xf
	v_mul_f32_e32 v69, v69, v241
	v_cvt_pk_bf16_f32 v69, v69, v228
	v_mul_f32_dpp v228, v70, v242 quad_perm:[1,0,3,2] row_mask:0xf bank_mask:0xf
	v_mul_f32_e32 v70, v70, v242
	v_cvt_pk_bf16_f32 v70, v70, v228
	v_mul_f32_dpp v228, v71, v243 quad_perm:[1,0,3,2] row_mask:0xf bank_mask:0xf
	v_mul_f32_e32 v71, v71, v243
	v_cvt_pk_bf16_f32 v71, v71, v228
	v_mul_f32_dpp v228, v72, v244 quad_perm:[1,0,3,2] row_mask:0xf bank_mask:0xf
	v_mul_f32_e32 v72, v72, v244
	v_cvt_pk_bf16_f32 v72, v72, v228
	v_mul_f32_dpp v228, v73, v245 quad_perm:[1,0,3,2] row_mask:0xf bank_mask:0xf
	v_mul_f32_e32 v73, v73, v245
	v_cvt_pk_bf16_f32 v73, v73, v228
	v_mul_f32_dpp v228, v74, v246 quad_perm:[1,0,3,2] row_mask:0xf bank_mask:0xf
	v_mul_f32_e32 v74, v74, v246
	v_cvt_pk_bf16_f32 v74, v74, v228
	v_mul_f32_dpp v228, v75, v247 quad_perm:[1,0,3,2] row_mask:0xf bank_mask:0xf
	v_mul_f32_e32 v75, v75, v247
	v_cvt_pk_bf16_f32 v75, v75, v228
	v_mul_f32_dpp v228, v76, v248 quad_perm:[1,0,3,2] row_mask:0xf bank_mask:0xf
	v_mul_f32_e32 v76, v76, v248
	v_cvt_pk_bf16_f32 v76, v76, v228
	v_mul_f32_dpp v228, v77, v249 quad_perm:[1,0,3,2] row_mask:0xf bank_mask:0xf
	v_mul_f32_e32 v77, v77, v249
	v_cvt_pk_bf16_f32 v77, v77, v228
	v_mul_f32_dpp v228, v78, v250 quad_perm:[1,0,3,2] row_mask:0xf bank_mask:0xf
	v_mul_f32_e32 v78, v78, v250
	v_cvt_pk_bf16_f32 v78, v78, v228
	v_mul_f32_dpp v228, v79, v251 quad_perm:[1,0,3,2] row_mask:0xf bank_mask:0xf
	v_mul_f32_e32 v79, v79, v251
	v_cvt_pk_bf16_f32 v79, v79, v228
	v_mul_f32_dpp v228, v80, v236 quad_perm:[1,0,3,2] row_mask:0xf bank_mask:0xf
	v_mul_f32_e32 v80, v80, v236
	v_cvt_pk_bf16_f32 v80, v80, v228
	v_mul_f32_dpp v228, v81, v237 quad_perm:[1,0,3,2] row_mask:0xf bank_mask:0xf
	v_mul_f32_e32 v81, v81, v237
	v_cvt_pk_bf16_f32 v81, v81, v228
	v_mul_f32_dpp v228, v82, v238 quad_perm:[1,0,3,2] row_mask:0xf bank_mask:0xf
	v_mul_f32_e32 v82, v82, v238
	v_cvt_pk_bf16_f32 v82, v82, v228
	v_mul_f32_dpp v228, v83, v239 quad_perm:[1,0,3,2] row_mask:0xf bank_mask:0xf
	v_mul_f32_e32 v83, v83, v239
	v_cvt_pk_bf16_f32 v83, v83, v228
	v_mul_f32_dpp v228, v84, v240 quad_perm:[1,0,3,2] row_mask:0xf bank_mask:0xf
	v_mul_f32_e32 v84, v84, v240
	v_cvt_pk_bf16_f32 v84, v84, v228
	v_mul_f32_dpp v228, v85, v241 quad_perm:[1,0,3,2] row_mask:0xf bank_mask:0xf
	v_mul_f32_e32 v85, v85, v241
	v_cvt_pk_bf16_f32 v85, v85, v228
	v_mul_f32_dpp v228, v86, v242 quad_perm:[1,0,3,2] row_mask:0xf bank_mask:0xf
	v_mul_f32_e32 v86, v86, v242
	v_cvt_pk_bf16_f32 v86, v86, v228
	v_mul_f32_dpp v228, v87, v243 quad_perm:[1,0,3,2] row_mask:0xf bank_mask:0xf
	v_mul_f32_e32 v87, v87, v243
	v_cvt_pk_bf16_f32 v87, v87, v228
	v_mul_f32_dpp v228, v88, v244 quad_perm:[1,0,3,2] row_mask:0xf bank_mask:0xf
	v_mul_f32_e32 v88, v88, v244
	v_cvt_pk_bf16_f32 v88, v88, v228
	v_mul_f32_dpp v228, v89, v245 quad_perm:[1,0,3,2] row_mask:0xf bank_mask:0xf
	v_mul_f32_e32 v89, v89, v245
	v_cvt_pk_bf16_f32 v89, v89, v228
	v_mul_f32_dpp v228, v90, v246 quad_perm:[1,0,3,2] row_mask:0xf bank_mask:0xf
	v_mul_f32_e32 v90, v90, v246
	v_cvt_pk_bf16_f32 v90, v90, v228
	v_mul_f32_dpp v228, v91, v247 quad_perm:[1,0,3,2] row_mask:0xf bank_mask:0xf
	v_mul_f32_e32 v91, v91, v247
	v_cvt_pk_bf16_f32 v91, v91, v228
	v_mul_f32_dpp v228, v92, v248 quad_perm:[1,0,3,2] row_mask:0xf bank_mask:0xf
	v_mul_f32_e32 v92, v92, v248
	v_cvt_pk_bf16_f32 v92, v92, v228
	v_mul_f32_dpp v228, v93, v249 quad_perm:[1,0,3,2] row_mask:0xf bank_mask:0xf
	v_mul_f32_e32 v93, v93, v249
	v_cvt_pk_bf16_f32 v93, v93, v228
	v_mul_f32_dpp v228, v94, v250 quad_perm:[1,0,3,2] row_mask:0xf bank_mask:0xf
	v_mul_f32_e32 v94, v94, v250
	v_cvt_pk_bf16_f32 v94, v94, v228
	v_mul_f32_dpp v228, v95, v251 quad_perm:[1,0,3,2] row_mask:0xf bank_mask:0xf
	v_mul_f32_e32 v95, v95, v251
	v_cvt_pk_bf16_f32 v95, v95, v228
	v_mul_f32_dpp v228, v98, v236 quad_perm:[1,0,3,2] row_mask:0xf bank_mask:0xf
	v_mul_f32_e32 v98, v98, v236
	v_cvt_pk_bf16_f32 v98, v98, v228
	v_mul_f32_dpp v228, v99, v237 quad_perm:[1,0,3,2] row_mask:0xf bank_mask:0xf
	v_mul_f32_e32 v99, v99, v237
	v_cvt_pk_bf16_f32 v99, v99, v228
	v_mul_f32_dpp v228, v100, v238 quad_perm:[1,0,3,2] row_mask:0xf bank_mask:0xf
	v_mul_f32_e32 v100, v100, v238
	v_cvt_pk_bf16_f32 v100, v100, v228
	v_mul_f32_dpp v228, v101, v239 quad_perm:[1,0,3,2] row_mask:0xf bank_mask:0xf
	v_mul_f32_e32 v101, v101, v239
	v_cvt_pk_bf16_f32 v101, v101, v228
	v_mul_f32_dpp v228, v102, v240 quad_perm:[1,0,3,2] row_mask:0xf bank_mask:0xf
	v_mul_f32_e32 v102, v102, v240
	v_cvt_pk_bf16_f32 v102, v102, v228
	v_mul_f32_dpp v228, v103, v241 quad_perm:[1,0,3,2] row_mask:0xf bank_mask:0xf
	v_mul_f32_e32 v103, v103, v241
	v_cvt_pk_bf16_f32 v103, v103, v228
	v_mul_f32_dpp v228, v104, v242 quad_perm:[1,0,3,2] row_mask:0xf bank_mask:0xf
	v_mul_f32_e32 v104, v104, v242
	v_cvt_pk_bf16_f32 v104, v104, v228
	v_mul_f32_dpp v228, v105, v243 quad_perm:[1,0,3,2] row_mask:0xf bank_mask:0xf
	v_mul_f32_e32 v105, v105, v243
	v_cvt_pk_bf16_f32 v105, v105, v228
	v_mul_f32_dpp v228, v106, v244 quad_perm:[1,0,3,2] row_mask:0xf bank_mask:0xf
	v_mul_f32_e32 v106, v106, v244
	v_cvt_pk_bf16_f32 v106, v106, v228
	v_mul_f32_dpp v228, v107, v245 quad_perm:[1,0,3,2] row_mask:0xf bank_mask:0xf
	v_mul_f32_e32 v107, v107, v245
	v_cvt_pk_bf16_f32 v107, v107, v228
	v_mul_f32_dpp v228, v108, v246 quad_perm:[1,0,3,2] row_mask:0xf bank_mask:0xf
	v_mul_f32_e32 v108, v108, v246
	v_cvt_pk_bf16_f32 v108, v108, v228
	v_mul_f32_dpp v228, v109, v247 quad_perm:[1,0,3,2] row_mask:0xf bank_mask:0xf
	v_mul_f32_e32 v109, v109, v247
	v_cvt_pk_bf16_f32 v109, v109, v228
	v_mul_f32_dpp v228, v110, v248 quad_perm:[1,0,3,2] row_mask:0xf bank_mask:0xf
	v_mul_f32_e32 v110, v110, v248
	v_cvt_pk_bf16_f32 v110, v110, v228
	v_mul_f32_dpp v228, v111, v249 quad_perm:[1,0,3,2] row_mask:0xf bank_mask:0xf
	v_mul_f32_e32 v111, v111, v249
	v_cvt_pk_bf16_f32 v111, v111, v228
	v_mul_f32_dpp v228, v112, v250 quad_perm:[1,0,3,2] row_mask:0xf bank_mask:0xf
	v_mul_f32_e32 v112, v112, v250
	v_cvt_pk_bf16_f32 v112, v112, v228
	v_mul_f32_dpp v228, v113, v251 quad_perm:[1,0,3,2] row_mask:0xf bank_mask:0xf
	v_mul_f32_e32 v113, v113, v251
	v_cvt_pk_bf16_f32 v113, v113, v228
	v_mul_f32_dpp v228, v114, v236 quad_perm:[1,0,3,2] row_mask:0xf bank_mask:0xf
	v_mul_f32_e32 v114, v114, v236
	v_cvt_pk_bf16_f32 v114, v114, v228
	v_mul_f32_dpp v228, v115, v237 quad_perm:[1,0,3,2] row_mask:0xf bank_mask:0xf
	v_mul_f32_e32 v115, v115, v237
	v_cvt_pk_bf16_f32 v115, v115, v228
	v_mul_f32_dpp v228, v116, v238 quad_perm:[1,0,3,2] row_mask:0xf bank_mask:0xf
	v_mul_f32_e32 v116, v116, v238
	v_cvt_pk_bf16_f32 v116, v116, v228
	v_mul_f32_dpp v228, v117, v239 quad_perm:[1,0,3,2] row_mask:0xf bank_mask:0xf
	v_mul_f32_e32 v117, v117, v239
	v_cvt_pk_bf16_f32 v117, v117, v228
	v_mul_f32_dpp v228, v118, v240 quad_perm:[1,0,3,2] row_mask:0xf bank_mask:0xf
	v_mul_f32_e32 v118, v118, v240
	v_cvt_pk_bf16_f32 v118, v118, v228
	v_mul_f32_dpp v228, v119, v241 quad_perm:[1,0,3,2] row_mask:0xf bank_mask:0xf
	v_mul_f32_e32 v119, v119, v241
	v_cvt_pk_bf16_f32 v119, v119, v228
	v_mul_f32_dpp v228, v120, v242 quad_perm:[1,0,3,2] row_mask:0xf bank_mask:0xf
	v_mul_f32_e32 v120, v120, v242
	v_cvt_pk_bf16_f32 v120, v120, v228
	v_mul_f32_dpp v228, v121, v243 quad_perm:[1,0,3,2] row_mask:0xf bank_mask:0xf
	v_mul_f32_e32 v121, v121, v243
	v_cvt_pk_bf16_f32 v121, v121, v228
	v_mul_f32_dpp v228, v122, v244 quad_perm:[1,0,3,2] row_mask:0xf bank_mask:0xf
	v_mul_f32_e32 v122, v122, v244
	v_cvt_pk_bf16_f32 v122, v122, v228
	v_mul_f32_dpp v228, v123, v245 quad_perm:[1,0,3,2] row_mask:0xf bank_mask:0xf
	v_mul_f32_e32 v123, v123, v245
	v_cvt_pk_bf16_f32 v123, v123, v228
	v_mul_f32_dpp v228, v124, v246 quad_perm:[1,0,3,2] row_mask:0xf bank_mask:0xf
	v_mul_f32_e32 v124, v124, v246
	v_cvt_pk_bf16_f32 v124, v124, v228
	v_mul_f32_dpp v228, v125, v247 quad_perm:[1,0,3,2] row_mask:0xf bank_mask:0xf
	v_mul_f32_e32 v125, v125, v247
	v_cvt_pk_bf16_f32 v125, v125, v228
	v_mul_f32_dpp v228, v126, v248 quad_perm:[1,0,3,2] row_mask:0xf bank_mask:0xf
	v_mul_f32_e32 v126, v126, v248
	v_cvt_pk_bf16_f32 v126, v126, v228
	v_mul_f32_dpp v228, v127, v249 quad_perm:[1,0,3,2] row_mask:0xf bank_mask:0xf
	v_mul_f32_e32 v127, v127, v249
	v_cvt_pk_bf16_f32 v127, v127, v228
	v_mul_f32_dpp v228, v128, v250 quad_perm:[1,0,3,2] row_mask:0xf bank_mask:0xf
	v_mul_f32_e32 v128, v128, v250
	v_cvt_pk_bf16_f32 v128, v128, v228
	v_mul_f32_dpp v228, v129, v251 quad_perm:[1,0,3,2] row_mask:0xf bank_mask:0xf
	v_mul_f32_e32 v129, v129, v251
	v_cvt_pk_bf16_f32 v129, v129, v228
	s_barrier
	s_lshl_b32 s21, s15, 13
	v_lshlrev_b32_e32 v233, 10, v229
	v_lshl_add_u32 v233, v231, 1, v233
	v_add_u32_e32 v233, s21, v233
	v_mbcnt_lo_u32_b32 v234, -1, 0
	v_mbcnt_hi_u32_b32 v234, -1, v234
	v_lshlrev_b32_e32 v234, 4, v234
	v_add_u32_e32 v230, s21, v234
	v_add_u32_e32 v232, 0x1000, v230
	v_add_u32_e32 v234, s21, v234
	s_mov_b64 s[48:49], exec
	s_mov_b32 s50, 0x55555555
	s_mov_b32 s51, 0x55555555
	s_mov_b64 exec, s[50:51]
	ds_write_b32 v233, v0 offset:0
	ds_write_b32 v233, v1 offset:256
	ds_write_b32 v233, v2 offset:512
	ds_write_b32 v233, v3 offset:768
	ds_write_b32 v233, v4 offset:2048
	ds_write_b32 v233, v5 offset:2304
	ds_write_b32 v233, v6 offset:2560
	ds_write_b32 v233, v7 offset:2816
	ds_write_b32 v233, v8 offset:4096
	ds_write_b32 v233, v9 offset:4352
	ds_write_b32 v233, v10 offset:4608
	ds_write_b32 v233, v11 offset:4864
	ds_write_b32 v233, v12 offset:6144
	ds_write_b32 v233, v13 offset:6400
	ds_write_b32 v233, v14 offset:6656
	ds_write_b32 v233, v15 offset:6912
	ds_write_b32 v233, v16 offset:64
	ds_write_b32 v233, v17 offset:320
	ds_write_b32 v233, v18 offset:576
	ds_write_b32 v233, v19 offset:832
	ds_write_b32 v233, v20 offset:2112
	ds_write_b32 v233, v21 offset:2368
	ds_write_b32 v233, v22 offset:2624
	ds_write_b32 v233, v23 offset:2880
	ds_write_b32 v233, v24 offset:4160
	ds_write_b32 v233, v25 offset:4416
	ds_write_b32 v233, v26 offset:4672
	ds_write_b32 v233, v27 offset:4928
	ds_write_b32 v233, v28 offset:6208
	ds_write_b32 v233, v29 offset:6464
	ds_write_b32 v233, v30 offset:6720
	ds_write_b32 v233, v31 offset:6976
	ds_write_b32 v233, v32 offset:128
	ds_write_b32 v233, v33 offset:384
	ds_write_b32 v233, v34 offset:640
	ds_write_b32 v233, v35 offset:896
	ds_write_b32 v233, v36 offset:2176
	ds_write_b32 v233, v37 offset:2432
	ds_write_b32 v233, v38 offset:2688
	ds_write_b32 v233, v39 offset:2944
	ds_write_b32 v233, v40 offset:4224
	ds_write_b32 v233, v41 offset:4480
	ds_write_b32 v233, v42 offset:4736
	ds_write_b32 v233, v43 offset:4992
	ds_write_b32 v233, v44 offset:6272
	ds_write_b32 v233, v45 offset:6528
	ds_write_b32 v233, v46 offset:6784
	ds_write_b32 v233, v47 offset:7040
	ds_write_b32 v233, v48 offset:192
	ds_write_b32 v233, v49 offset:448
	ds_write_b32 v233, v50 offset:704
	ds_write_b32 v233, v51 offset:960
	ds_write_b32 v233, v52 offset:2240
	ds_write_b32 v233, v53 offset:2496
	ds_write_b32 v233, v54 offset:2752
	ds_write_b32 v233, v55 offset:3008
	ds_write_b32 v233, v56 offset:4288
	ds_write_b32 v233, v57 offset:4544
	ds_write_b32 v233, v58 offset:4800
	ds_write_b32 v233, v59 offset:5056
	ds_write_b32 v233, v60 offset:6336
	ds_write_b32 v233, v61 offset:6592
	ds_write_b32 v233, v62 offset:6848
	ds_write_b32 v233, v63 offset:7104
	s_mov_b64 exec, s[48:49]
	s_waitcnt lgkmcnt(0)
	ds_read_b128 v[236:239], v234 offset:0
	ds_read_b128 v[240:243], v234 offset:1024
	ds_read_b128 v[244:247], v234 offset:2048
	ds_read_b128 v[248:251], v234 offset:3072
	ds_read_b128 v[194:197], v234 offset:4096
	ds_read_b128 v[198:201], v234 offset:5120
	ds_read_b128 v[212:215], v234 offset:6144
	ds_read_b128 v[216:219], v234 offset:7168
	s_waitcnt lgkmcnt(0)
	global_store_dwordx4 v230, v[236:239], s[42:43] offset:0
	global_store_dwordx4 v230, v[240:243], s[42:43] offset:1024
	global_store_dwordx4 v230, v[244:247], s[42:43] offset:2048
	global_store_dwordx4 v230, v[248:251], s[42:43] offset:3072
	global_store_dwordx4 v232, v[194:197], s[42:43] offset:0
	global_store_dwordx4 v232, v[198:201], s[42:43] offset:1024
	global_store_dwordx4 v232, v[212:215], s[42:43] offset:2048
	global_store_dwordx4 v232, v[216:219], s[42:43] offset:3072
	s_nop 1
	s_mov_b64 exec, s[50:51]
	ds_write_b32 v233, v64 offset:0
	ds_write_b32 v233, v65 offset:256
	ds_write_b32 v233, v66 offset:512
	ds_write_b32 v233, v67 offset:768
	ds_write_b32 v233, v68 offset:2048
	ds_write_b32 v233, v69 offset:2304
	ds_write_b32 v233, v70 offset:2560
	ds_write_b32 v233, v71 offset:2816
	ds_write_b32 v233, v72 offset:4096
	ds_write_b32 v233, v73 offset:4352
	ds_write_b32 v233, v74 offset:4608
	ds_write_b32 v233, v75 offset:4864
	ds_write_b32 v233, v76 offset:6144
	ds_write_b32 v233, v77 offset:6400
	ds_write_b32 v233, v78 offset:6656
	ds_write_b32 v233, v79 offset:6912
	ds_write_b32 v233, v80 offset:64
	ds_write_b32 v233, v81 offset:320
	ds_write_b32 v233, v82 offset:576
	ds_write_b32 v233, v83 offset:832
	ds_write_b32 v233, v84 offset:2112
	ds_write_b32 v233, v85 offset:2368
	ds_write_b32 v233, v86 offset:2624
	ds_write_b32 v233, v87 offset:2880
	ds_write_b32 v233, v88 offset:4160
	ds_write_b32 v233, v89 offset:4416
	ds_write_b32 v233, v90 offset:4672
	ds_write_b32 v233, v91 offset:4928
	ds_write_b32 v233, v92 offset:6208
	ds_write_b32 v233, v93 offset:6464
	ds_write_b32 v233, v94 offset:6720
	ds_write_b32 v233, v95 offset:6976
	ds_write_b32 v233, v98 offset:128
	ds_write_b32 v233, v99 offset:384
	ds_write_b32 v233, v100 offset:640
	ds_write_b32 v233, v101 offset:896
	ds_write_b32 v233, v102 offset:2176
	ds_write_b32 v233, v103 offset:2432
	ds_write_b32 v233, v104 offset:2688
	ds_write_b32 v233, v105 offset:2944
	ds_write_b32 v233, v106 offset:4224
	ds_write_b32 v233, v107 offset:4480
	ds_write_b32 v233, v108 offset:4736
	ds_write_b32 v233, v109 offset:4992
	ds_write_b32 v233, v110 offset:6272
	ds_write_b32 v233, v111 offset:6528
	ds_write_b32 v233, v112 offset:6784
	ds_write_b32 v233, v113 offset:7040
	ds_write_b32 v233, v114 offset:192
	ds_write_b32 v233, v115 offset:448
	ds_write_b32 v233, v116 offset:704
	ds_write_b32 v233, v117 offset:960
	ds_write_b32 v233, v118 offset:2240
	ds_write_b32 v233, v119 offset:2496
	ds_write_b32 v233, v120 offset:2752
	ds_write_b32 v233, v121 offset:3008
	ds_write_b32 v233, v122 offset:4288
	ds_write_b32 v233, v123 offset:4544
	ds_write_b32 v233, v124 offset:4800
	ds_write_b32 v233, v125 offset:5056
	ds_write_b32 v233, v126 offset:6336
	ds_write_b32 v233, v127 offset:6592
	ds_write_b32 v233, v128 offset:6848
	ds_write_b32 v233, v129 offset:7104
	s_mov_b64 exec, s[48:49]
	s_waitcnt lgkmcnt(0)
	ds_read_b128 v[236:239], v234 offset:0
	ds_read_b128 v[240:243], v234 offset:1024
	ds_read_b128 v[244:247], v234 offset:2048
	ds_read_b128 v[248:251], v234 offset:3072
	ds_read_b128 v[194:197], v234 offset:4096
	ds_read_b128 v[198:201], v234 offset:5120
	ds_read_b128 v[212:215], v234 offset:6144
	ds_read_b128 v[216:219], v234 offset:7168
	s_waitcnt lgkmcnt(0)
	global_store_dwordx4 v230, v[236:239], s[44:45] offset:0
	global_store_dwordx4 v230, v[240:243], s[44:45] offset:1024
	global_store_dwordx4 v230, v[244:247], s[44:45] offset:2048
	global_store_dwordx4 v230, v[248:251], s[44:45] offset:3072
	global_store_dwordx4 v232, v[194:197], s[44:45] offset:0
	global_store_dwordx4 v232, v[198:201], s[44:45] offset:1024
	global_store_dwordx4 v232, v[212:215], s[44:45] offset:2048
	global_store_dwordx4 v232, v[216:219], s[44:45] offset:3072
	s_nop 1
	s_barrier
	s_branch .Lfa_epi_done
